# P8: skip MFMAs of 16x16 output blocks without a selected pair (mask from next unit's slot words fetched in the epilogue)
# speedup vs baseline: 1.0179x; 1.0070x over previous
.LBB0_930:
	v_readlane_b32 s10, v254, 0
	v_readlane_b32 s11, v254, 1
	s_load_dwordx2 s[10:11], s[10:11], 0xa0
	s_mov_b64 s[12:13], 0x80
	v_lshl_add_u64 v[6:7], v[6:7], 0, s[12:13]
	s_waitcnt vmcnt(2)
	s_barrier
	s_waitcnt lgkmcnt(0)
	s_add_u32 s10, s10, 0x55400000
	s_addc_u32 s11, s11, 0
	s_add_i32 s51, s33, 0x18000
	s_lshl_b32 s5, s94, 12
	s_mov_b32 m0, s51
	s_add_i32 s52, s33, 0x1a000
	s_lshl_b32 s16, s4, 13
	s_and_b32 s5, s5, 0x3000
	global_load_lds_dwordx4 v[6:7], off
	v_lshl_add_u64 v[4:5], v[4:5], 0, s[12:13]
	s_mov_b32 m0, s52
	s_add_i32 s53, s33, 0x8000
	s_add_i32 s54, s33, 0xa000
	global_load_lds_dwordx4 v[4:5], off
	v_lshl_add_u64 v[0:1], v[0:1], 0, s[12:13]
	s_mov_b32 m0, s53
	s_add_u32 s14, s40, 0x80080
	global_load_lds_dwordx4 v[0:1], off
	v_lshl_add_u64 v[0:1], v[2:3], 0, s[12:13]
	s_mov_b32 m0, s54
	s_addc_u32 s15, s41, 0
	s_add_i32 s55, s33, 0x1c000
	global_load_lds_dwordx4 v[0:1], off
	v_lshl_add_u64 v[0:1], s[14:15], 0, v[162:163]
	s_mov_b32 m0, s55
	s_add_i32 s56, s33, 0x1e000
	global_load_lds_dwordx4 v[0:1], off
	v_lshl_add_u64 v[0:1], s[14:15], 0, v[166:167]
	s_mov_b32 m0, s56
	v_lshlrev_b32_e32 v4, 2, v14
	global_load_lds_dwordx4 v[0:1], off
	v_lshrrev_b32_e32 v0, 1, v14
	v_and_b32_e32 v1, 15, v14
	v_and_b32_e32 v0, 24, v0
	v_lshlrev_b32_e32 v2, 1, v0
	v_lshlrev_b32_e32 v3, 6, v1
	v_and_b32_e32 v4, 32, v4
	s_add_i32 s5, s5, 0
	v_bitop3_b32 v2, v3, v4, v2 bitop3:0x36
	s_cmpk_lt_u32 s65, 0x100
	v_lshl_or_b32 v188, s4, 6, v1
	v_add_u32_e32 v3, s5, v2
	s_cselect_b64 s[14:15], -1, 0
	s_lshl_b64 s[4:5], s[94:95], 9
	s_ashr_i32 s57, s64, 31
	s_ashr_i32 s58, s68, 31
	v_readlane_b32 s18, v254, 14
	v_readlane_b32 s19, v254, 15
	s_add_u32 s4, s18, s4
	v_lshlrev_b32_e32 v168, 5, v1
	s_addc_u32 s5, s19, s5
	v_add_u32_e32 v4, 0, v2
	v_mov_b32_e32 v1, v169
	v_add_u32_e32 v189, 0x10000, v3
	v_add_u32_e32 v190, 0x10400, v3
	v_add_u32_e32 v191, 0x10800, v3
	v_add_u32_e32 v192, 0x10c00, v3
	v_add_u32_e32 v193, 0x14000, v3
	v_add_u32_e32 v194, 0x14400, v3
	v_add_u32_e32 v195, 0x14800, v3
	v_add_u32_e32 v196, 0x14c00, v3
	v_add_u32_e32 v197, 0x18000, v3
	v_add_u32_e32 v198, 0x18400, v3
	v_add_u32_e32 v199, 0x18800, v3
	v_add_u32_e32 v200, 0x18c00, v3
	v_add_u32_e32 v201, 0x1c000, v3
	v_add_u32_e32 v202, 0x1c400, v3
	v_add_u32_e32 v203, 0x1c800, v3
	v_add_u32_e32 v204, 0x1cc00, v3
	v_lshl_add_u64 v[2:3], s[4:5], 0, v[168:169]
	v_lshl_add_u64 v[170:171], v[2:3], 0, v[0:1]
	v_lshlrev_b32_e32 v0, 15, v8
	v_and_b32_e32 v0, 0xffff0000, v0
	v_lshl_add_u32 v0, v9, 12, v0
	v_and_b32_e32 v1, 1, v8
	v_lshl_or_b32 v0, v1, 6, v0
	v_lshl_add_u32 v172, v10, 1, v0
	v_lshlrev_b32_e32 v0, 15, v11
	v_and_b32_e32 v0, 0xffff0000, v0
	s_waitcnt vmcnt(6)
	v_lshl_add_u32 v0, v12, 12, v0
	v_and_b32_e32 v1, 1, v11
	v_lshl_or_b32 v0, v1, 6, v0
	v_mov_b32_e32 v173, v169
	v_lshl_add_u32 v174, v13, 1, v0
	v_mov_b32_e32 v175, v169
	v_mov_b64_e32 v[176:177], 0x1000
	v_mov_b64_e32 v[178:179], 0xfff
	v_add_u32_e32 v205, s16, v4
	s_mov_b32 s59, 0xffffff
	s_mov_b64 s[16:17], 0x10000
	s_mov_b64 s[18:19], 0x12000
	s_mov_b64 s[20:21], 0x14000
	s_mov_b64 s[22:23], 0x16000
	v_mov_b32_e32 v206, 2
	s_barrier
	s_mov_b32 s74, -1
	s_branch .LBB0_933

.LBB0_940:
	s_add_u32 s72, s38, 0xfff80000
	s_addc_u32 s73, s39, -1
	s_mov_b32 m0, s53
	s_nop 0
	global_load_lds_dwordx4 v160, s[72:73]
	s_mov_b32 m0, s54
	s_nop 0
	global_load_lds_dwordx4 v164, s[72:73]
	ds_read_b128 v[16:19], v189
	ds_read_b128 v[20:23], v190
	ds_read_b128 v[24:27], v191
	ds_read_b128 v[28:31], v192
	ds_read_b128 v[0:3], v193
	ds_read_b128 v[4:7], v194
	ds_read_b128 v[8:11], v195
	ds_read_b128 v[12:15], v196
	s_add_u32 s40, s38, 0xfff80080
	s_addc_u32 s41, s39, -1
	s_cmp_eq_u32 s64, 28
	s_cselect_b32 s43, s27, s41
	s_cselect_b32 s42, s35, s40
	s_cselect_b32 s41, s25, s61
	s_cselect_b32 s40, s37, s60
	s_add_i32 m0, s33, 0xc000
	ds_read_b128 v[180:183], v205
	ds_read_b128 v[184:187], v205 offset:1024
	ds_read_b128 v[208:211], v205 offset:2048
	ds_read_b128 v[212:215], v205 offset:3072
	ds_read_b128 v[216:219], v205 offset:4096
	ds_read_b128 v[220:223], v205 offset:5120
	ds_read_b128 v[224:227], v205 offset:6144
	ds_read_b128 v[228:231], v205 offset:7168
	global_load_lds_dwordx4 v172, s[38:39]
	s_add_i32 m0, s33, 0xe000
	s_nop 0
	global_load_lds_dwordx4 v174, s[38:39]
	s_waitcnt vmcnt(8)
	s_waitcnt lgkmcnt(0)
	s_barrier
	s_setprio 1
	s_waitcnt lgkmcnt(0)
	s_bitcmp1_b32 s74, 0
	s_cbranch_scc0 .Lp8s_0
	v_mfma_f32_16x16x128_f8f6f4 v[156:159], v[16:23], v[180:187], v[156:159]
.Lp8s_0:
	s_bitcmp1_b32 s74, 1
	s_cbranch_scc0 .Lp8s_1
	v_mfma_f32_16x16x128_f8f6f4 v[152:155], v[24:31], v[180:187], v[152:155]
.Lp8s_1:
	s_bitcmp1_b32 s74, 4
	s_cbranch_scc0 .Lp8s_2
	v_mfma_f32_16x16x128_f8f6f4 v[140:143], v[16:23], v[208:215], v[140:143]
.Lp8s_2:
	s_bitcmp1_b32 s74, 5
	s_cbranch_scc0 .Lp8s_3
	v_mfma_f32_16x16x128_f8f6f4 v[136:139], v[24:31], v[208:215], v[136:139]
.Lp8s_3:
	s_bitcmp1_b32 s74, 8
	s_cbranch_scc0 .Lp8s_4
	v_mfma_f32_16x16x128_f8f6f4 v[124:127], v[16:23], v[216:223], v[124:127]
.Lp8s_4:
	s_bitcmp1_b32 s74, 9
	s_cbranch_scc0 .Lp8s_5
	v_mfma_f32_16x16x128_f8f6f4 v[120:123], v[24:31], v[216:223], v[120:123]
.Lp8s_5:
	s_bitcmp1_b32 s74, 12
	s_cbranch_scc0 .Lp8s_6
	v_mfma_f32_16x16x128_f8f6f4 v[108:111], v[16:23], v[224:231], v[108:111]
.Lp8s_6:
	s_bitcmp1_b32 s74, 13
	s_cbranch_scc0 .Lp8s_7
	v_mfma_f32_16x16x128_f8f6f4 v[104:107], v[24:31], v[224:231], v[104:107]
.Lp8s_7:
	s_setprio 0
	s_setprio 1
	s_bitcmp1_b32 s74, 2
	s_cbranch_scc0 .Lp8s_8
	v_mfma_f32_16x16x128_f8f6f4 v[148:151], v[0:7], v[180:187], v[148:151]
.Lp8s_8:
	s_bitcmp1_b32 s74, 3
	s_cbranch_scc0 .Lp8s_9
	v_mfma_f32_16x16x128_f8f6f4 v[144:147], v[8:15], v[180:187], v[144:147]
.Lp8s_9:
	s_bitcmp1_b32 s74, 6
	s_cbranch_scc0 .Lp8s_10
	v_mfma_f32_16x16x128_f8f6f4 v[132:135], v[0:7], v[208:215], v[132:135]
.Lp8s_10:
	s_bitcmp1_b32 s74, 7
	s_cbranch_scc0 .Lp8s_11
	v_mfma_f32_16x16x128_f8f6f4 v[128:131], v[8:15], v[208:215], v[128:131]
.Lp8s_11:
	s_bitcmp1_b32 s74, 10
	s_cbranch_scc0 .Lp8s_12
	v_mfma_f32_16x16x128_f8f6f4 v[116:119], v[0:7], v[216:223], v[116:119]
.Lp8s_12:
	s_bitcmp1_b32 s74, 11
	s_cbranch_scc0 .Lp8s_13
	v_mfma_f32_16x16x128_f8f6f4 v[112:115], v[8:15], v[216:223], v[112:115]
.Lp8s_13:
	s_bitcmp1_b32 s74, 14
	s_cbranch_scc0 .Lp8s_14
	v_mfma_f32_16x16x128_f8f6f4 v[100:103], v[0:7], v[224:231], v[100:103]
.Lp8s_14:
	s_bitcmp1_b32 s74, 15
	s_cbranch_scc0 .Lp8s_15
	v_mfma_f32_16x16x128_f8f6f4 v[96:99], v[8:15], v[224:231], v[96:99]
.Lp8s_15:
	s_setprio 0
	s_barrier
	s_mov_b32 m0, s44
	v_lshl_add_u64 v[180:181], s[40:41], 0, v[162:163]
	s_add_u32 s62, s40, 0x80000
	ds_read_b128 v[208:211], v205 offset:16384
	ds_read_b128 v[212:215], v205 offset:17408
	ds_read_b128 v[216:219], v205 offset:18432
	ds_read_b128 v[220:223], v205 offset:19456
	ds_read_b128 v[224:227], v205 offset:20480
	ds_read_b128 v[228:231], v205 offset:21504
	ds_read_b128 v[232:235], v205 offset:22528
	ds_read_b128 v[236:239], v205 offset:23552
	global_load_lds_dwordx4 v[180:181], off
	v_lshl_add_u64 v[182:183], s[40:41], 0, v[166:167]
	s_mov_b32 m0, s45
	s_addc_u32 s63, s41, 0
	global_load_lds_dwordx4 v[182:183], off
	s_mov_b32 m0, s46
	s_nop 0
	global_load_lds_dwordx4 v162, s[62:63]
	s_mov_b32 m0, s47
	s_nop 0
	global_load_lds_dwordx4 v166, s[62:63]
	s_waitcnt vmcnt(6)
	s_waitcnt lgkmcnt(0)
	s_barrier
	s_setprio 1
	s_waitcnt lgkmcnt(0)
	s_bitcmp1_b32 s74, 16
	s_cbranch_scc0 .Lp8s_16
	v_mfma_f32_16x16x128_f8f6f4 v[92:95], v[16:23], v[208:215], v[92:95]
.Lp8s_16:
	s_bitcmp1_b32 s74, 17
	s_cbranch_scc0 .Lp8s_17
	v_mfma_f32_16x16x128_f8f6f4 v[88:91], v[24:31], v[208:215], v[88:91]
.Lp8s_17:
	s_bitcmp1_b32 s74, 20
	s_cbranch_scc0 .Lp8s_18
	v_mfma_f32_16x16x128_f8f6f4 v[76:79], v[16:23], v[216:223], v[76:79]
.Lp8s_18:
	s_bitcmp1_b32 s74, 21
	s_cbranch_scc0 .Lp8s_19
	v_mfma_f32_16x16x128_f8f6f4 v[72:75], v[24:31], v[216:223], v[72:75]
.Lp8s_19:
	s_bitcmp1_b32 s74, 24
	s_cbranch_scc0 .Lp8s_20
	v_mfma_f32_16x16x128_f8f6f4 v[60:63], v[16:23], v[224:231], v[60:63]
.Lp8s_20:
	s_bitcmp1_b32 s74, 25
	s_cbranch_scc0 .Lp8s_21
	v_mfma_f32_16x16x128_f8f6f4 v[56:59], v[24:31], v[224:231], v[56:59]
.Lp8s_21:
	s_bitcmp1_b32 s74, 28
	s_cbranch_scc0 .Lp8s_22
	v_mfma_f32_16x16x128_f8f6f4 v[44:47], v[16:23], v[232:239], v[44:47]
.Lp8s_22:
	s_bitcmp1_b32 s74, 29
	s_cbranch_scc0 .Lp8s_23
	v_mfma_f32_16x16x128_f8f6f4 v[40:43], v[24:31], v[232:239], v[40:43]
.Lp8s_23:
	s_setprio 0
	s_setprio 1
	s_bitcmp1_b32 s74, 18
	s_cbranch_scc0 .Lp8s_24
	v_mfma_f32_16x16x128_f8f6f4 v[84:87], v[0:7], v[208:215], v[84:87]
.Lp8s_24:
	s_bitcmp1_b32 s74, 19
	s_cbranch_scc0 .Lp8s_25
	v_mfma_f32_16x16x128_f8f6f4 v[80:83], v[8:15], v[208:215], v[80:83]
.Lp8s_25:
	s_bitcmp1_b32 s74, 22
	s_cbranch_scc0 .Lp8s_26
	v_mfma_f32_16x16x128_f8f6f4 v[68:71], v[0:7], v[216:223], v[68:71]
.Lp8s_26:
	s_bitcmp1_b32 s74, 23
	s_cbranch_scc0 .Lp8s_27
	v_mfma_f32_16x16x128_f8f6f4 v[64:67], v[8:15], v[216:223], v[64:67]
.Lp8s_27:
	s_bitcmp1_b32 s74, 26
	s_cbranch_scc0 .Lp8s_28
	v_mfma_f32_16x16x128_f8f6f4 v[52:55], v[0:7], v[224:231], v[52:55]
.Lp8s_28:
	s_bitcmp1_b32 s74, 27
	s_cbranch_scc0 .Lp8s_29
	v_mfma_f32_16x16x128_f8f6f4 v[48:51], v[8:15], v[224:231], v[48:51]
.Lp8s_29:
	s_bitcmp1_b32 s74, 30
	s_cbranch_scc0 .Lp8s_30
	v_mfma_f32_16x16x128_f8f6f4 v[36:39], v[0:7], v[232:239], v[36:39]
.Lp8s_30:
	s_bitcmp1_b32 s74, 31
	s_cbranch_scc0 .Lp8s_31
	v_mfma_f32_16x16x128_f8f6f4 v[32:35], v[8:15], v[232:239], v[32:35]
.Lp8s_31:
	s_setprio 0
	s_barrier
	s_mov_b32 m0, s33
	s_nop 0
	global_load_lds_dwordx4 v160, s[42:43]
	s_mov_b32 m0, s48
	s_nop 0
	global_load_lds_dwordx4 v164, s[42:43]
	ds_read_b128 v[0:3], v197
	ds_read_b128 v[4:7], v198
	ds_read_b128 v[8:11], v199
	ds_read_b128 v[12:15], v200
	ds_read_b128 v[16:19], v201
	ds_read_b128 v[20:23], v202
	ds_read_b128 v[24:27], v203
	ds_read_b128 v[28:31], v204
	s_add_u32 s42, s42, 0x80000
	s_addc_u32 s43, s43, 0
	s_mov_b32 m0, s49
	ds_read_b128 v[208:211], v205 offset:32768
	ds_read_b128 v[212:215], v205 offset:33792
	ds_read_b128 v[216:219], v205 offset:34816
	ds_read_b128 v[220:223], v205 offset:35840
	ds_read_b128 v[224:227], v205 offset:36864
	ds_read_b128 v[228:231], v205 offset:37888
	ds_read_b128 v[232:235], v205 offset:38912
	ds_read_b128 v[236:239], v205 offset:39936
	global_load_lds_dwordx4 v160, s[42:43]
	s_mov_b32 m0, s50
	s_nop 0
	global_load_lds_dwordx4 v164, s[42:43]
	s_waitcnt vmcnt(8)
	s_waitcnt lgkmcnt(0)
	s_barrier
	s_setprio 1
	s_waitcnt lgkmcnt(0)
	s_bitcmp1_b32 s74, 0
	s_cbranch_scc0 .Lp8s_32
	v_mfma_f32_16x16x128_f8f6f4 v[156:159], v[0:7], v[208:215], v[156:159]
.Lp8s_32:
	s_bitcmp1_b32 s74, 1
	s_cbranch_scc0 .Lp8s_33
	v_mfma_f32_16x16x128_f8f6f4 v[152:155], v[8:15], v[208:215], v[152:155]
.Lp8s_33:
	s_bitcmp1_b32 s74, 4
	s_cbranch_scc0 .Lp8s_34
	v_mfma_f32_16x16x128_f8f6f4 v[140:143], v[0:7], v[216:223], v[140:143]
.Lp8s_34:
	s_bitcmp1_b32 s74, 5
	s_cbranch_scc0 .Lp8s_35
	v_mfma_f32_16x16x128_f8f6f4 v[136:139], v[8:15], v[216:223], v[136:139]
.Lp8s_35:
	s_bitcmp1_b32 s74, 8
	s_cbranch_scc0 .Lp8s_36
	v_mfma_f32_16x16x128_f8f6f4 v[124:127], v[0:7], v[224:231], v[124:127]
.Lp8s_36:
	s_bitcmp1_b32 s74, 9
	s_cbranch_scc0 .Lp8s_37
	v_mfma_f32_16x16x128_f8f6f4 v[120:123], v[8:15], v[224:231], v[120:123]
.Lp8s_37:
	s_bitcmp1_b32 s74, 12
	s_cbranch_scc0 .Lp8s_38
	v_mfma_f32_16x16x128_f8f6f4 v[108:111], v[0:7], v[232:239], v[108:111]
.Lp8s_38:
	s_bitcmp1_b32 s74, 13
	s_cbranch_scc0 .Lp8s_39
	v_mfma_f32_16x16x128_f8f6f4 v[104:107], v[8:15], v[232:239], v[104:107]
.Lp8s_39:
	s_setprio 0
	s_setprio 1
	s_bitcmp1_b32 s74, 2
	s_cbranch_scc0 .Lp8s_40
	v_mfma_f32_16x16x128_f8f6f4 v[148:151], v[16:23], v[208:215], v[148:151]
.Lp8s_40:
	s_bitcmp1_b32 s74, 3
	s_cbranch_scc0 .Lp8s_41
	v_mfma_f32_16x16x128_f8f6f4 v[144:147], v[24:31], v[208:215], v[144:147]
.Lp8s_41:
	s_bitcmp1_b32 s74, 6
	s_cbranch_scc0 .Lp8s_42
	v_mfma_f32_16x16x128_f8f6f4 v[132:135], v[16:23], v[216:223], v[132:135]
.Lp8s_42:
	s_bitcmp1_b32 s74, 7
	s_cbranch_scc0 .Lp8s_43
	v_mfma_f32_16x16x128_f8f6f4 v[128:131], v[24:31], v[216:223], v[128:131]
.Lp8s_43:
	s_bitcmp1_b32 s74, 10
	s_cbranch_scc0 .Lp8s_44
	v_mfma_f32_16x16x128_f8f6f4 v[116:119], v[16:23], v[224:231], v[116:119]
.Lp8s_44:
	s_bitcmp1_b32 s74, 11
	s_cbranch_scc0 .Lp8s_45
	v_mfma_f32_16x16x128_f8f6f4 v[112:115], v[24:31], v[224:231], v[112:115]
.Lp8s_45:
	s_bitcmp1_b32 s74, 14
	s_cbranch_scc0 .Lp8s_46
	v_mfma_f32_16x16x128_f8f6f4 v[100:103], v[16:23], v[232:239], v[100:103]
.Lp8s_46:
	s_bitcmp1_b32 s74, 15
	s_cbranch_scc0 .Lp8s_47
	v_mfma_f32_16x16x128_f8f6f4 v[96:99], v[24:31], v[232:239], v[96:99]
.Lp8s_47:
	s_setprio 0
	s_barrier
	s_mov_b32 m0, s51
	v_lshl_add_u64 v[180:181], v[180:181], 0, s[12:13]
	s_add_u32 s40, s40, 0x80080
	ds_read_b128 v[208:211], v205 offset:49152
	ds_read_b128 v[212:215], v205 offset:50176
	ds_read_b128 v[216:219], v205 offset:51200
	ds_read_b128 v[220:223], v205 offset:52224
	ds_read_b128 v[224:227], v205 offset:53248
	ds_read_b128 v[228:231], v205 offset:54272
	ds_read_b128 v[232:235], v205 offset:55296
	ds_read_b128 v[236:239], v205 offset:56320
	global_load_lds_dwordx4 v[180:181], off
	v_lshl_add_u64 v[180:181], v[182:183], 0, s[12:13]
	s_mov_b32 m0, s52
	s_addc_u32 s41, s41, 0
	global_load_lds_dwordx4 v[180:181], off
	s_mov_b32 m0, s55
	s_nop 0
	global_load_lds_dwordx4 v162, s[40:41]
	s_mov_b32 m0, s56
	s_nop 0
	global_load_lds_dwordx4 v166, s[40:41]
	s_waitcnt vmcnt(6)
	s_waitcnt lgkmcnt(0)
	s_barrier
	s_setprio 1
	s_waitcnt lgkmcnt(0)
	s_bitcmp1_b32 s74, 16
	s_cbranch_scc0 .Lp8s_48
	v_mfma_f32_16x16x128_f8f6f4 v[92:95], v[0:7], v[208:215], v[92:95]
.Lp8s_48:
	s_bitcmp1_b32 s74, 17
	s_cbranch_scc0 .Lp8s_49
	v_mfma_f32_16x16x128_f8f6f4 v[88:91], v[8:15], v[208:215], v[88:91]
.Lp8s_49:
	s_bitcmp1_b32 s74, 20
	s_cbranch_scc0 .Lp8s_50
	v_mfma_f32_16x16x128_f8f6f4 v[76:79], v[0:7], v[216:223], v[76:79]
.Lp8s_50:
	s_bitcmp1_b32 s74, 21
	s_cbranch_scc0 .Lp8s_51
	v_mfma_f32_16x16x128_f8f6f4 v[72:75], v[8:15], v[216:223], v[72:75]
.Lp8s_51:
	s_bitcmp1_b32 s74, 24
	s_cbranch_scc0 .Lp8s_52
	v_mfma_f32_16x16x128_f8f6f4 v[60:63], v[0:7], v[224:231], v[60:63]
.Lp8s_52:
	s_bitcmp1_b32 s74, 25
	s_cbranch_scc0 .Lp8s_53
	v_mfma_f32_16x16x128_f8f6f4 v[56:59], v[8:15], v[224:231], v[56:59]
.Lp8s_53:
	s_bitcmp1_b32 s74, 28
	s_cbranch_scc0 .Lp8s_54
	v_mfma_f32_16x16x128_f8f6f4 v[44:47], v[0:7], v[232:239], v[44:47]
.Lp8s_54:
	s_bitcmp1_b32 s74, 29
	s_cbranch_scc0 .Lp8s_55
	v_mfma_f32_16x16x128_f8f6f4 v[40:43], v[8:15], v[232:239], v[40:43]
.Lp8s_55:
	s_setprio 0
	s_setprio 1
	s_bitcmp1_b32 s74, 18
	s_cbranch_scc0 .Lp8s_56
	v_mfma_f32_16x16x128_f8f6f4 v[84:87], v[16:23], v[208:215], v[84:87]
.Lp8s_56:
	s_bitcmp1_b32 s74, 19
	s_cbranch_scc0 .Lp8s_57
	v_mfma_f32_16x16x128_f8f6f4 v[80:83], v[24:31], v[208:215], v[80:83]
.Lp8s_57:
	s_bitcmp1_b32 s74, 22
	s_cbranch_scc0 .Lp8s_58
	v_mfma_f32_16x16x128_f8f6f4 v[68:71], v[16:23], v[216:223], v[68:71]
.Lp8s_58:
	s_bitcmp1_b32 s74, 23
	s_cbranch_scc0 .Lp8s_59
	v_mfma_f32_16x16x128_f8f6f4 v[64:67], v[24:31], v[216:223], v[64:67]
.Lp8s_59:
	s_bitcmp1_b32 s74, 26
	s_cbranch_scc0 .Lp8s_60
	v_mfma_f32_16x16x128_f8f6f4 v[52:55], v[16:23], v[224:231], v[52:55]
.Lp8s_60:
	s_bitcmp1_b32 s74, 27
	s_cbranch_scc0 .Lp8s_61
	v_mfma_f32_16x16x128_f8f6f4 v[48:51], v[24:31], v[224:231], v[48:51]
.Lp8s_61:
	s_bitcmp1_b32 s74, 30
	s_cbranch_scc0 .Lp8s_62
	v_mfma_f32_16x16x128_f8f6f4 v[36:39], v[16:23], v[232:239], v[36:39]
.Lp8s_62:
	s_bitcmp1_b32 s74, 31
	s_cbranch_scc0 .Lp8s_63
	v_mfma_f32_16x16x128_f8f6f4 v[32:35], v[24:31], v[232:239], v[32:35]
.Lp8s_63:
	s_setprio 0
	s_barrier
	s_add_i32 s64, s64, 2
	s_add_u32 s38, s38, 0x100
	s_addc_u32 s39, s39, 0
	s_add_u32 s60, s60, 0x100
	s_addc_u32 s61, s61, 0
	s_cmp_gt_u32 s64, 29
	s_cbranch_scc0 .LBB0_940
	s_nop 15
	s_nop 15
	s_and_b64 vcc, exec, s[14:15]
	s_cbranch_vccz .LBB0_943
	s_barrier
.LBB0_943:
	s_mov_b32 s75, -1
	s_cmp_lg_u64 s[4:5], 0
	s_cbranch_scc0 .Lp8n_skip
	s_lshl_b32 s76, s26, 6
	s_add_i32 s76, s76, s24
	s_ashr_i32 s77, s76, 31
	s_lshl_b64 s[76:77], s[76:77], 16
	v_lshl_add_u64 v[186:187], v[170:171], 0, s[76:77]
	s_mov_b64 s[76:77], 0x1000
	global_load_dwordx2 v[208:209], v[186:187], off
	v_lshl_add_u64 v[186:187], v[186:187], 0, s[76:77]
	global_load_dwordx2 v[210:211], v[186:187], off
	v_lshl_add_u64 v[186:187], v[186:187], 0, s[76:77]
	global_load_dwordx2 v[212:213], v[186:187], off
	v_lshl_add_u64 v[186:187], v[186:187], 0, s[76:77]
	global_load_dwordx2 v[214:215], v[186:187], off
	v_lshl_add_u64 v[186:187], v[186:187], 0, s[76:77]
	global_load_dwordx2 v[216:217], v[186:187], off
	v_lshl_add_u64 v[186:187], v[186:187], 0, s[76:77]
	global_load_dwordx2 v[218:219], v[186:187], off
	v_lshl_add_u64 v[186:187], v[186:187], 0, s[76:77]
	global_load_dwordx2 v[220:221], v[186:187], off
	v_lshl_add_u64 v[186:187], v[186:187], 0, s[76:77]
	global_load_dwordx2 v[222:223], v[186:187], off
	v_lshl_add_u64 v[186:187], v[186:187], 0, s[76:77]
	global_load_dwordx2 v[224:225], v[186:187], off
	v_lshl_add_u64 v[186:187], v[186:187], 0, s[76:77]
	global_load_dwordx2 v[226:227], v[186:187], off
	v_lshl_add_u64 v[186:187], v[186:187], 0, s[76:77]
	global_load_dwordx2 v[228:229], v[186:187], off
	v_lshl_add_u64 v[186:187], v[186:187], 0, s[76:77]
	global_load_dwordx2 v[230:231], v[186:187], off
	v_lshl_add_u64 v[186:187], v[186:187], 0, s[76:77]
	global_load_dwordx2 v[232:233], v[186:187], off
	v_lshl_add_u64 v[186:187], v[186:187], 0, s[76:77]
	global_load_dwordx2 v[234:235], v[186:187], off
	v_lshl_add_u64 v[186:187], v[186:187], 0, s[76:77]
	global_load_dwordx2 v[236:237], v[186:187], off
	v_lshl_add_u64 v[186:187], v[186:187], 0, s[76:77]
	global_load_dwordx2 v[238:239], v[186:187], off
.Lp8n_skip:
	s_lshl_b32 s25, s34, 6
	s_add_i32 s36, s25, s36
	s_ashr_i32 s37, s36, 31
	s_lshl_b64 s[36:37], s[36:37], 16
	v_lshl_add_u64 v[0:1], v[170:171], 0, s[36:37]
	v_add_co_u32_e32 v2, vcc, 0x1000, v0
	s_nop 1
	v_addc_co_u32_e32 v3, vcc, 0, v1, vcc
	v_add_co_u32_e32 v4, vcc, 0x2000, v0
	s_nop 1
	v_addc_co_u32_e32 v5, vcc, 0, v1, vcc
	v_add_co_u32_e32 v6, vcc, 0x3000, v0
	s_nop 1
	v_addc_co_u32_e32 v7, vcc, 0, v1, vcc
	global_load_dwordx2 v[182:183], v[0:1], off
	global_load_dwordx2 v[30:31], v[2:3], off
	global_load_dwordx2 v[28:29], v[4:5], off
	global_load_dwordx2 v[26:27], v[6:7], off
	v_add_co_u32_e32 v2, vcc, 0x4000, v0
	s_nop 1
	v_addc_co_u32_e32 v3, vcc, 0, v1, vcc
	v_add_co_u32_e32 v4, vcc, 0x5000, v0
	s_nop 1
	v_addc_co_u32_e32 v5, vcc, 0, v1, vcc
	v_add_co_u32_e32 v6, vcc, 0x6000, v0
	s_nop 1
	v_addc_co_u32_e32 v7, vcc, 0, v1, vcc
	v_add_co_u32_e32 v8, vcc, 0x7000, v0
	s_nop 1
	v_addc_co_u32_e32 v9, vcc, 0, v1, vcc
	global_load_dwordx2 v[24:25], v[2:3], off
	global_load_dwordx2 v[22:23], v[4:5], off
	global_load_dwordx2 v[20:21], v[6:7], off
	global_load_dwordx2 v[18:19], v[8:9], off
	v_add_co_u32_e32 v2, vcc, 0x8000, v0
	s_nop 1
	v_addc_co_u32_e32 v3, vcc, 0, v1, vcc
	v_add_co_u32_e32 v4, vcc, 0x9000, v0
	s_nop 1
	v_addc_co_u32_e32 v5, vcc, 0, v1, vcc
	v_add_co_u32_e32 v6, vcc, 0xa000, v0
	s_nop 1
	v_addc_co_u32_e32 v7, vcc, 0, v1, vcc
	v_add_co_u32_e32 v8, vcc, 0xb000, v0
	s_nop 1
	v_addc_co_u32_e32 v9, vcc, 0, v1, vcc
	global_load_dwordx2 v[16:17], v[2:3], off
	global_load_dwordx2 v[14:15], v[4:5], off
	global_load_dwordx2 v[12:13], v[6:7], off
	global_load_dwordx2 v[10:11], v[8:9], off
	v_add_co_u32_e32 v2, vcc, 0xc000, v0
	s_nop 1
	v_addc_co_u32_e32 v3, vcc, 0, v1, vcc
	v_add_co_u32_e32 v4, vcc, 0xd000, v0
	s_nop 1
	v_addc_co_u32_e32 v5, vcc, 0, v1, vcc
	v_add_co_u32_e32 v180, vcc, 0xe000, v0
	s_nop 1
	v_addc_co_u32_e32 v181, vcc, 0, v1, vcc
	v_add_co_u32_e32 v0, vcc, 0xf000, v0
	s_nop 1
	v_addc_co_u32_e32 v1, vcc, 0, v1, vcc
	global_load_dwordx2 v[8:9], v[2:3], off
	global_load_dwordx2 v[6:7], v[4:5], off
	s_nop 0
	global_load_dwordx2 v[2:3], v[180:181], off
	s_nop 0
	global_load_dwordx2 v[0:1], v[0:1], off
	v_lshl_add_u32 v4, s34, 8, v188
	v_ashrrev_i32_e32 v5, 31, v4
	v_lshlrev_b64 v[180:181], 9, v[4:5]
	v_lshl_add_u64 v[180:181], s[10:11], 0, v[180:181]
	s_waitcnt vmcnt(0)
	s_cmp_lg_u64 s[4:5], 0
	s_cbranch_scc0 .Lp8m_skip
	s_mov_b32 s75, 0
	v_cmp_ne_u32_e64 s[76:77], 0, v208
	s_cmp_lg_u64 s[76:77], 0
	s_cselect_b32 s78, 0x1, 0
	s_or_b32 s75, s75, s78
	v_cmp_ne_u32_e64 s[76:77], 0, v209
	s_cmp_lg_u64 s[76:77], 0
	s_cselect_b32 s78, 0x2, 0
	s_or_b32 s75, s75, s78
	v_cmp_ne_u32_e64 s[76:77], 0, v210
	s_cmp_lg_u64 s[76:77], 0
	s_cselect_b32 s78, 0x4, 0
	s_or_b32 s75, s75, s78
	v_cmp_ne_u32_e64 s[76:77], 0, v211
	s_cmp_lg_u64 s[76:77], 0
	s_cselect_b32 s78, 0x8, 0
	s_or_b32 s75, s75, s78
	v_cmp_ne_u32_e64 s[76:77], 0, v212
	s_cmp_lg_u64 s[76:77], 0
	s_cselect_b32 s78, 0x10, 0
	s_or_b32 s75, s75, s78
	v_cmp_ne_u32_e64 s[76:77], 0, v213
	s_cmp_lg_u64 s[76:77], 0
	s_cselect_b32 s78, 0x20, 0
	s_or_b32 s75, s75, s78
	v_cmp_ne_u32_e64 s[76:77], 0, v214
	s_cmp_lg_u64 s[76:77], 0
	s_cselect_b32 s78, 0x40, 0
	s_or_b32 s75, s75, s78
	v_cmp_ne_u32_e64 s[76:77], 0, v215
	s_cmp_lg_u64 s[76:77], 0
	s_cselect_b32 s78, 0x80, 0
	s_or_b32 s75, s75, s78
	v_cmp_ne_u32_e64 s[76:77], 0, v216
	s_cmp_lg_u64 s[76:77], 0
	s_cselect_b32 s78, 0x100, 0
	s_or_b32 s75, s75, s78
	v_cmp_ne_u32_e64 s[76:77], 0, v217
	s_cmp_lg_u64 s[76:77], 0
	s_cselect_b32 s78, 0x200, 0
	s_or_b32 s75, s75, s78
	v_cmp_ne_u32_e64 s[76:77], 0, v218
	s_cmp_lg_u64 s[76:77], 0
	s_cselect_b32 s78, 0x400, 0
	s_or_b32 s75, s75, s78
	v_cmp_ne_u32_e64 s[76:77], 0, v219
	s_cmp_lg_u64 s[76:77], 0
	s_cselect_b32 s78, 0x800, 0
	s_or_b32 s75, s75, s78
	v_cmp_ne_u32_e64 s[76:77], 0, v220
	s_cmp_lg_u64 s[76:77], 0
	s_cselect_b32 s78, 0x1000, 0
	s_or_b32 s75, s75, s78
	v_cmp_ne_u32_e64 s[76:77], 0, v221
	s_cmp_lg_u64 s[76:77], 0
	s_cselect_b32 s78, 0x2000, 0
	s_or_b32 s75, s75, s78
	v_cmp_ne_u32_e64 s[76:77], 0, v222
	s_cmp_lg_u64 s[76:77], 0
	s_cselect_b32 s78, 0x4000, 0
	s_or_b32 s75, s75, s78
	v_cmp_ne_u32_e64 s[76:77], 0, v223
	s_cmp_lg_u64 s[76:77], 0
	s_cselect_b32 s78, 0x8000, 0
	s_or_b32 s75, s75, s78
	v_cmp_ne_u32_e64 s[76:77], 0, v224
	s_cmp_lg_u64 s[76:77], 0
	s_cselect_b32 s78, 0x10000, 0
	s_or_b32 s75, s75, s78
	v_cmp_ne_u32_e64 s[76:77], 0, v225
	s_cmp_lg_u64 s[76:77], 0
	s_cselect_b32 s78, 0x20000, 0
	s_or_b32 s75, s75, s78
	v_cmp_ne_u32_e64 s[76:77], 0, v226
	s_cmp_lg_u64 s[76:77], 0
	s_cselect_b32 s78, 0x40000, 0
	s_or_b32 s75, s75, s78
	v_cmp_ne_u32_e64 s[76:77], 0, v227
	s_cmp_lg_u64 s[76:77], 0
	s_cselect_b32 s78, 0x80000, 0
	s_or_b32 s75, s75, s78
	v_cmp_ne_u32_e64 s[76:77], 0, v228
	s_cmp_lg_u64 s[76:77], 0
	s_cselect_b32 s78, 0x100000, 0
	s_or_b32 s75, s75, s78
	v_cmp_ne_u32_e64 s[76:77], 0, v229
	s_cmp_lg_u64 s[76:77], 0
	s_cselect_b32 s78, 0x200000, 0
	s_or_b32 s75, s75, s78
	v_cmp_ne_u32_e64 s[76:77], 0, v230
	s_cmp_lg_u64 s[76:77], 0
	s_cselect_b32 s78, 0x400000, 0
	s_or_b32 s75, s75, s78
	v_cmp_ne_u32_e64 s[76:77], 0, v231
	s_cmp_lg_u64 s[76:77], 0
	s_cselect_b32 s78, 0x800000, 0
	s_or_b32 s75, s75, s78
	v_cmp_ne_u32_e64 s[76:77], 0, v232
	s_cmp_lg_u64 s[76:77], 0
	s_cselect_b32 s78, 0x1000000, 0
	s_or_b32 s75, s75, s78
	v_cmp_ne_u32_e64 s[76:77], 0, v233
	s_cmp_lg_u64 s[76:77], 0
	s_cselect_b32 s78, 0x2000000, 0
	s_or_b32 s75, s75, s78
	v_cmp_ne_u32_e64 s[76:77], 0, v234
	s_cmp_lg_u64 s[76:77], 0
	s_cselect_b32 s78, 0x4000000, 0
	s_or_b32 s75, s75, s78
	v_cmp_ne_u32_e64 s[76:77], 0, v235
	s_cmp_lg_u64 s[76:77], 0
	s_cselect_b32 s78, 0x8000000, 0
	s_or_b32 s75, s75, s78
	v_cmp_ne_u32_e64 s[76:77], 0, v236
	s_cmp_lg_u64 s[76:77], 0
	s_cselect_b32 s78, 0x10000000, 0
	s_or_b32 s75, s75, s78
	v_cmp_ne_u32_e64 s[76:77], 0, v237
	s_cmp_lg_u64 s[76:77], 0
	s_cselect_b32 s78, 0x20000000, 0
	s_or_b32 s75, s75, s78
	v_cmp_ne_u32_e64 s[76:77], 0, v238
	s_cmp_lg_u64 s[76:77], 0
	s_cselect_b32 s78, 0x40000000, 0
	s_or_b32 s75, s75, s78
	v_cmp_ne_u32_e64 s[76:77], 0, v239
	s_cmp_lg_u64 s[76:77], 0
	s_cselect_b32 s78, 0x80000000, 0
	s_or_b32 s75, s75, s78
.Lp8m_skip:
	v_or_b32_e32 v168, v182, v183
	v_cmp_ne_u32_e32 vcc, 0, v168
	s_and_saveexec_b64 s[34:35], vcc
	s_mov_b32 s64, s66
	s_cbranch_execz .LBB0_953
	v_cmp_ne_u32_sdwa s[38:39], v182, v169 src0_sel:BYTE_0 src1_sel:DWORD
	s_and_saveexec_b64 s[36:37], s[38:39]
	s_cbranch_execnz .LBB0_1106
	s_or_b64 exec, exec, s[36:37]
	v_cmp_ne_u32_sdwa s[38:39], v182, v169 src0_sel:BYTE_1 src1_sel:DWORD
	s_and_saveexec_b64 s[36:37], s[38:39]
	s_cbranch_execnz .LBB0_1107

.LBB0_1103:
	s_or_b64 exec, exec, s[34:35]
	s_mov_b32 s74, s75
	s_andn2_b64 vcc, exec, s[4:5]
	s_mov_b64 s[4:5], -1
	s_cbranch_vccnz .LBB0_932
	s_andn2_b64 vcc, exec, s[8:9]
	s_cbranch_vccnz .LBB0_931
	s_barrier
	s_branch .LBB0_931
